# tail
# speedup vs baseline: 1.1200x; 1.0110x over previous
.LBB1_12:
	s_and_b32 s12, s19, 1
	s_lshr_b32 s13, s19, 1
	s_add_i32 s16, s19, 1
	v_lshl_add_u32 v231, s13, 3, v221
	s_cmp_lg_u32 s19, 3
	s_cselect_b32 s17, s16, 3
	s_waitcnt lgkmcnt(2)
	v_lshlrev_b32_e32 v2, 7, v231
	s_lshl_b32 s14, s12, 6
	v_or3_b32 v160, v2, s14, v220
	s_waitcnt lgkmcnt(0)
	v_mov_b32_e32 v1, v220
	v_lshl_add_u64 v[2:3], v[160:161], 2, s[6:7]
	global_load_dword v232, v[2:3], off
	s_lshl_b32 s14, s17, 2
	s_and_b32 s14, s14, 24
	s_lshl_b32 s13, s13, 9
	v_lshrrev_b32_e32 v3, 5, v1
	s_cmp_eq_u32 s12, 0
	v_add_u32_e32 v2, s14, v221
	v_lshlrev_b32_e32 v206, 4, v3
	s_cselect_b64 s[14:15], -1, 0
	s_cmp_eq_u32 s12, 1
	v_add3_u32 v149, v228, s13, v206
	s_cselect_b64 s[12:13], -1, 0
	s_lshl_b32 s17, s17, 6
	s_and_b32 s17, s17, 64
	v_lshl_or_b32 v2, v2, 7, s17
	v_lshl_add_u32 v234, v1, 4, 0
	v_and_or_b32 v1, v1, 31, v2
	v_mul_lo_u32 v2, v1, 27
	v_add_u32_e32 v233, 0xc000, v234
	v_mad_u64_u32 v[204:205], s[20:21], v3, 14, v[2:3]
	v_add_u32_e32 v202, 13, v2
	s_waitcnt vmcnt(3)
	v_mul_f32_e32 v1, 0.15915494, v222
	v_cos_f32_e32 v2, v1
	v_sin_f32_e32 v1, v1
	v_add_f32_e32 v2, v2, v2
	v_cndmask_b32_e64 v3, v2, v1, s[0:1]
	v_mul_f32_e32 v1, v1, v2
	v_fma_f32 v2, v2, v2, -2.0
	v_cndmask_b32_e64 v4, v2, v1, s[0:1]
	v_mul_f32_e32 v207, v1, v2
	v_fma_f32 v208, v2, v2, -2.0
	v_mul_f32_e32 v2, 0.15915494, v182
	v_cvt_pk_fp8_f32 v131, v225, v3
	v_cos_f32_e32 v3, v2
	v_sin_f32_e32 v2, v2
	v_cndmask_b32_e64 v1, v208, v207, s[0:1]
	v_cvt_pk_fp8_f32 v131, v4, v1 op_sel:[0,0,1]
	v_add_f32_e32 v1, v3, v3
	v_cvt_pk_f16_f32 v1, v2, v1
	v_cvt_pk_fp8_f32 v128, v182, v0
	v_cvt_scalef32_pk_fp8_f16 v132, v1, 1.0
	v_pk_fma_f16 v1, v1, v1, -2.0 op_sel:[1,0,1] op_sel_hi:[1,1,0]
	v_mul_f32_e32 v0, 0.15915494, v0
	v_cvt_scalef32_pk_fp8_f16 v132, v1, 1.0 op_sel:[0,0,1]
	v_pk_fma_f16 v1, v1, v1, -2.0 op_sel:[0,1,1] op_sel_hi:[1,1,0]
	v_cos_f32_e32 v2, v0
	v_cvt_scalef32_pk_fp8_f16 v133, v1, 1.0
	v_pk_fma_f16 v1, v1, v1, -2.0 op_sel:[0,1,1] op_sel_hi:[1,1,0]
	v_sin_f32_e32 v0, v0
	v_cvt_scalef32_pk_fp8_f16 v133, v1, 1.0 op_sel:[0,0,1]
	v_pk_fma_f16 v1, v1, v1, -2.0 op_sel:[0,1,1] op_sel_hi:[1,1,0]
	s_nop 0
	v_cvt_scalef32_pk_fp8_f16 v134, v1, 1.0
	v_pk_fma_f16 v1, v1, v1, -2.0 op_sel:[0,1,1] op_sel_hi:[1,1,0]
	s_nop 0
	v_cvt_scalef32_pk_fp8_f16 v134, v1, 1.0 op_sel:[0,0,1]
	v_add_f32_e32 v1, v2, v2
	v_cvt_pk_f16_f32 v0, v0, v1
	v_cvt_scalef32_pk_fp8_f16 v135, v0, 1.0
	v_pk_fma_f16 v24, v0, v0, -2.0 op_sel:[1,0,1] op_sel_hi:[1,1,0]
	s_waitcnt vmcnt(2)
	v_mul_f32_e32 v0, 0.15915494, v224
	v_cos_f32_e32 v1, v0
	v_sin_f32_e32 v0, v0
	v_add_f32_e32 v1, v1, v1
	v_cndmask_b32_e64 v2, v1, v0, s[0:1]
	v_mul_f32_e32 v0, v0, v1
	v_fma_f32 v1, v1, v1, -2.0
	v_cndmask_b32_e64 v3, v1, v0, s[0:1]
	v_mul_f32_e32 v209, v0, v1
	v_fma_f32 v210, v1, v1, -2.0
	v_mul_f32_e32 v1, 0.15915494, v190
	s_waitcnt vmcnt(1)
	v_cvt_pk_fp8_f32 v19, v223, v2
	v_cos_f32_e32 v2, v1
	v_sin_f32_e32 v1, v1
	v_cndmask_b32_e64 v0, v210, v209, s[0:1]
	v_cvt_pk_fp8_f32 v19, v3, v0 op_sel:[0,0,1]
	v_add_f32_e32 v0, v2, v2
	v_cvt_pk_f16_f32 v0, v1, v0
	v_cvt_scalef32_pk_fp8_f16 v20, v0, 1.0
	v_pk_fma_f16 v0, v0, v0, -2.0 op_sel:[1,0,1] op_sel_hi:[1,1,0]
	v_mul_f32_e32 v1, 0.15915494, v191
	v_cvt_scalef32_pk_fp8_f16 v135, v24, 1.0 op_sel:[0,0,1]
	v_cvt_scalef32_pk_fp8_f16 v20, v0, 1.0 op_sel:[0,0,1]
	v_pk_fma_f16 v0, v0, v0, -2.0 op_sel:[0,1,1] op_sel_hi:[1,1,0]
	v_cos_f32_e32 v2, v1
	v_pk_fma_f16 v24, v24, v24, -2.0 op_sel:[0,1,1] op_sel_hi:[1,1,0]
	v_cvt_scalef32_pk_fp8_f16 v21, v0, 1.0
	v_pk_fma_f16 v0, v0, v0, -2.0 op_sel:[0,1,1] op_sel_hi:[1,1,0]
	v_sin_f32_e32 v1, v1
	v_pk_fma_f16 v35, v24, v24, -2.0 op_sel:[0,1,1] op_sel_hi:[1,1,0]
	v_cvt_pk_fp8_f32 v128, v25, v185 op_sel:[0,0,1]
	v_cvt_scalef32_pk_fp8_f16 v21, v0, 1.0 op_sel:[0,0,1]
	v_pk_fma_f16 v0, v0, v0, -2.0 op_sel:[0,1,1] op_sel_hi:[1,1,0]
	v_pk_fma_f16 v36, v35, v35, -2.0 op_sel:[0,1,1] op_sel_hi:[1,1,0]
	v_mul_f32_e32 v25, 0.15915494, v25
	v_cvt_pk_fp8_f32 v129, v198, v162
	v_cvt_pk_fp8_f32 v130, v178, v200
	v_cvt_pk_fp8_f32 v16, v190, v191
	v_cvt_pk_fp8_f32 v17, v194, v195
	v_cvt_pk_fp8_f32 v18, v186, v187
	v_cvt_scalef32_pk_fp8_f16 v22, v0, 1.0
	v_pk_fma_f16 v0, v0, v0, -2.0 op_sel:[0,1,1] op_sel_hi:[1,1,0]
	v_pk_fma_f16 v37, v36, v36, -2.0 op_sel:[0,1,1] op_sel_hi:[1,1,0]
	v_cvt_scalef32_pk_fp8_f16 v137, v36, 1.0
	v_cos_f32_e32 v36, v25
	v_cvt_scalef32_pk_fp8_f16 v22, v0, 1.0 op_sel:[0,0,1]
	v_add_f32_e32 v0, v2, v2
	v_sin_f32_e32 v25, v25
	v_cvt_pk_f16_f32 v0, v1, v0
	v_mov_b32_e32 v160, v204
	v_cvt_scalef32_pk_fp8_f16 v23, v0, 1.0
	v_pk_fma_f16 v34, v0, v0, -2.0 op_sel:[1,0,1] op_sel_hi:[1,1,0]
	ds_read_b128 v[26:29], v234
	ds_read_b128 v[30:33], v234 offset:1024
	ds_read_b128 v[8:11], v234 offset:2048
	ds_read_b128 v[12:15], v234 offset:3072
	ds_read_b128 v[0:3], v234 offset:4096
	ds_read_b128 v[4:7], v234 offset:5120
	ds_read_b128 v[152:155], v234 offset:6144
	ds_read_b128 v[156:159], v234 offset:7168
	ds_read_b128 v[96:99], v149
	ds_read_b128 v[100:103], v149 offset:32
	ds_read_b128 v[104:107], v149 offset:64
	ds_read_b128 v[108:111], v149 offset:96
	v_cvt_pk_fp8_f32 v129, v163, v201 op_sel:[0,0,1]
	v_cvt_pk_fp8_f32 v130, v179, v181 op_sel:[0,0,1]
	v_cvt_pk_fp8_f32 v16, v192, v193 op_sel:[0,0,1]
	v_cvt_pk_fp8_f32 v17, v196, v197 op_sel:[0,0,1]
	v_cvt_pk_fp8_f32 v18, v188, v189 op_sel:[0,0,1]
	v_cvt_scalef32_pk_fp8_f16 v136, v24, 1.0
	v_add_f32_e32 v24, v36, v36
	v_cvt_pk_f16_f32 v24, v25, v24
	v_pk_fma_f16 v25, v24, v24, -2.0 op_sel:[1,0,1] op_sel_hi:[1,1,0]
	v_cvt_scalef32_pk_fp8_f16 v138, v24, 1.0
	v_cvt_scalef32_pk_fp8_f16 v23, v34, 1.0 op_sel:[0,0,1]
	v_cvt_scalef32_pk_fp8_f16 v136, v35, 1.0 op_sel:[0,0,1]
	v_pk_fma_f16 v35, v25, v25, -2.0 op_sel:[0,1,1] op_sel_hi:[1,1,0]
	v_cvt_scalef32_pk_fp8_f16 v138, v25, 1.0 op_sel:[0,0,1]
	v_mul_f32_e32 v25, 0.15915494, v185
	s_waitcnt lgkmcnt(0)
	v_mfma_scale_f32_32x32x64_f8f6f4 v[112:127], v[26:33], v[16:23], v[96:111], v227, v226 op_sel_hi:[0,0,0]
	v_cvt_scalef32_pk_fp8_f16 v139, v35, 1.0
	v_pk_fma_f16 v35, v35, v35, -2.0 op_sel:[0,1,1] op_sel_hi:[1,1,0]
	s_nop 0
	v_pk_fma_f16 v24, v35, v35, -2.0 op_sel:[0,1,1] op_sel_hi:[1,1,0]
	ds_read_b128 v[64:67], v149 offset:128
	ds_read_b128 v[68:71], v149 offset:160
	ds_read_b128 v[72:75], v149 offset:192
	ds_read_b128 v[76:79], v149 offset:224
	v_cvt_scalef32_pk_fp8_f16 v140, v24, 1.0
	v_pk_fma_f16 v24, v24, v24, -2.0 op_sel:[0,1,1] op_sel_hi:[1,1,0]
	v_cvt_scalef32_pk_fp8_f16 v137, v37, 1.0 op_sel:[0,0,1]
	v_cvt_scalef32_pk_fp8_f16 v140, v24, 1.0 op_sel:[0,0,1]
	v_cvt_scalef32_pk_fp8_f16 v139, v35, 1.0 op_sel:[0,0,1]
	v_mfma_scale_f32_32x32x64_f8f6f4 v[96:111], v[26:33], v[128:135], v[96:111], v227, v226 op_sel_hi:[0,0,0]
	v_cos_f32_e32 v26, v25
	v_sin_f32_e32 v25, v25
	v_mul_f32_e32 v30, 0.15915494, v192
	v_mul_f32_e32 v31, 0.15915494, v193
	v_add_f32_e32 v24, v26, v26
	v_cvt_pk_f16_f32 v24, v25, v24
	v_cvt_scalef32_pk_fp8_f16 v141, v24, 1.0
	v_pk_fma_f16 v24, v24, v24, -2.0 op_sel:[1,0,1] op_sel_hi:[1,1,0]
	s_nop 0
	v_cvt_scalef32_pk_fp8_f16 v141, v24, 1.0 op_sel:[0,0,1]
	v_pk_fma_f16 v26, v24, v24, -2.0 op_sel:[0,1,1] op_sel_hi:[1,1,0]
	v_lshl_add_u64 v[24:25], v[160:161], 2, s[4:5]
	v_pk_fma_f16 v27, v26, v26, -2.0 op_sel:[0,1,1] op_sel_hi:[1,1,0]
	s_nop 0
	v_pk_fma_f16 v28, v27, v27, -2.0 op_sel:[0,1,1] op_sel_hi:[1,1,0]
	s_waitcnt lgkmcnt(0)
	v_mfma_scale_f32_32x32x64_f8f6f4 v[80:95], v[8:15], v[16:23], v[64:79], v227, v226 op_sel_hi:[0,0,0]
	global_load_dwordx4 v[182:185], v[24:25], off
	global_load_dwordx4 v[190:193], v[24:25], off offset:3456
	v_cos_f32_e32 v25, v31
	v_pk_fma_f16 v29, v28, v28, -2.0 op_sel:[0,1,1] op_sel_hi:[1,1,0]
	v_cvt_scalef32_pk_fp8_f16 v143, v28, 1.0
	v_cvt_scalef32_pk_fp8_f16 v142, v26, 1.0
	v_cvt_scalef32_pk_fp8_f16 v143, v29, 1.0 op_sel:[0,0,1]
	v_cvt_scalef32_pk_fp8_f16 v142, v27, 1.0 op_sel:[0,0,1]
	v_add_f32_e32 v150, v25, v25
	v_mfma_scale_f32_32x32x64_f8f6f4 v[64:79], v[8:15], v[128:135], v[64:79], v227, v226 op_sel_hi:[0,0,0]
	v_pk_fma_f16 v8, v34, v34, -2.0 op_sel:[0,1,1] op_sel_hi:[1,1,0]
	ds_read_b128 v[32:35], v149 offset:256
	ds_read_b128 v[36:39], v149 offset:288
	ds_read_b128 v[40:43], v149 offset:320
	ds_read_b128 v[44:47], v149 offset:352
	v_pk_fma_f16 v9, v8, v8, -2.0 op_sel:[0,1,1] op_sel_hi:[1,1,0]
	v_cvt_scalef32_pk_fp8_f16 v144, v8, 1.0
	v_pk_fma_f16 v10, v9, v9, -2.0 op_sel:[0,1,1] op_sel_hi:[1,1,0]
	v_cvt_scalef32_pk_fp8_f16 v144, v9, 1.0 op_sel:[0,0,1]
	v_pk_fma_f16 v11, v10, v10, -2.0 op_sel:[0,1,1] op_sel_hi:[1,1,0]
	v_cvt_scalef32_pk_fp8_f16 v145, v10, 1.0
	v_cos_f32_e32 v10, v30
	v_cvt_scalef32_pk_fp8_f16 v145, v11, 1.0 op_sel:[0,0,1]
	v_sin_f32_e32 v11, v30
	v_add_f32_e32 v8, v10, v10
	v_cvt_pk_f16_f32 v8, v11, v8
	v_pk_fma_f16 v9, v8, v8, -2.0 op_sel:[1,0,1] op_sel_hi:[1,1,0]
	v_cvt_scalef32_pk_fp8_f16 v146, v8, 1.0
	v_pk_fma_f16 v10, v9, v9, -2.0 op_sel:[0,1,1] op_sel_hi:[1,1,0]
	s_waitcnt lgkmcnt(0)
	v_mfma_scale_f32_32x32x64_f8f6f4 v[48:63], v[0:7], v[16:23], v[32:47], v227, v226 op_sel_hi:[0,0,0]
	v_cvt_scalef32_pk_fp8_f16 v147, v10, 1.0
	v_pk_fma_f16 v10, v10, v10, -2.0 op_sel:[0,1,1] op_sel_hi:[1,1,0]
	v_cvt_scalef32_pk_fp8_f16 v146, v9, 1.0 op_sel:[0,0,1]
	v_cvt_scalef32_pk_fp8_f16 v147, v10, 1.0 op_sel:[0,0,1]
	v_pk_fma_f16 v24, v10, v10, -2.0 op_sel:[0,1,1] op_sel_hi:[1,1,0]
	s_nop 0
	v_cvt_scalef32_pk_fp8_f16 v148, v24, 1.0
	v_pk_fma_f16 v24, v24, v24, -2.0 op_sel:[0,1,1] op_sel_hi:[1,1,0]
	s_nop 0
	v_cvt_scalef32_pk_fp8_f16 v148, v24, 1.0 op_sel:[0,0,1]
	v_mfma_scale_f32_32x32x64_f8f6f4 v[32:47], v[0:7], v[128:135], v[32:47], v227, v226 op_sel_hi:[0,0,0]
	ds_read_b128 v[0:3], v149 offset:384
	ds_read_b128 v[4:7], v149 offset:416
	ds_read_b128 v[8:11], v149 offset:448
	ds_read_b128 v[12:15], v149 offset:480
	v_sin_f32_e32 v149, v31
	s_nop 0
	v_cvt_pk_f16_f32 v150, v149, v150
	v_cvt_scalef32_pk_fp8_f16 v149, v150, 1.0
	v_pk_fma_f16 v150, v150, v150, -2.0 op_sel:[1,0,1] op_sel_hi:[1,1,0]
	s_nop 0
	v_pk_fma_f16 v160, v150, v150, -2.0 op_sel:[0,1,1] op_sel_hi:[1,1,0]
	v_cvt_scalef32_pk_fp8_f16 v149, v150, 1.0 op_sel:[0,0,1]
	v_pk_fma_f16 v164, v160, v160, -2.0 op_sel:[0,1,1] op_sel_hi:[1,1,0]
	s_nop 0
	v_pk_fma_f16 v150, v164, v164, -2.0 op_sel:[0,1,1] op_sel_hi:[1,1,0]
	s_waitcnt lgkmcnt(0)
	v_mfma_scale_f32_32x32x64_f8f6f4 v[16:31], v[152:159], v[16:23], v[0:15], v227, v226 op_sel_hi:[0,0,0]
	v_pk_fma_f16 v165, v150, v150, -2.0 op_sel:[0,1,1] op_sel_hi:[1,1,0]
	v_cvt_scalef32_pk_fp8_f16 v151, v150, 1.0
	v_cvt_scalef32_pk_fp8_f16 v150, v160, 1.0
	v_cvt_scalef32_pk_fp8_f16 v151, v165, 1.0 op_sel:[0,0,1]
	v_cvt_scalef32_pk_fp8_f16 v150, v164, 1.0 op_sel:[0,0,1]
	v_mfma_scale_f32_32x32x64_f8f6f4 v[0:15], v[152:159], v[128:135], v[0:15], v227, v226 op_sel_hi:[0,0,0]
	v_mul_f32_e32 v128, 0.15915494, v198
	v_cos_f32_e32 v129, v128
	v_sin_f32_e32 v128, v128
	v_mul_f32_e32 v133, 0.15915494, v162
	v_cos_f32_e32 v134, v133
	v_add_f32_e32 v129, v129, v129
	v_cvt_pk_f16_f32 v130, v128, v129
	v_pk_fma_f16 v131, v130, v130, -2.0 op_sel:[1,0,1] op_sel_hi:[1,1,0]
	v_sin_f32_e32 v133, v133
	v_pk_fma_f16 v128, v131, v131, -2.0 op_sel:[0,1,1] op_sel_hi:[1,1,0]
	s_nop 0
	v_pk_fma_f16 v132, v128, v128, -2.0 op_sel:[0,1,1] op_sel_hi:[1,1,0]
	v_cvt_scalef32_pk_fp8_f16 v129, v128, 1.0
	v_cvt_scalef32_pk_fp8_f16 v128, v130, 1.0
	v_add_f32_e32 v130, v134, v134
	v_cvt_scalef32_pk_fp8_f16 v128, v131, 1.0 op_sel:[0,0,1]
	v_cvt_pk_f16_f32 v130, v133, v130
	v_cvt_scalef32_pk_fp8_f16 v129, v132, 1.0 op_sel:[0,0,1]
	v_cvt_scalef32_pk_fp8_f16 v131, v130, 1.0
	v_pk_fma_f16 v133, v130, v130, -2.0 op_sel:[1,0,1] op_sel_hi:[1,1,0]
	v_pk_fma_f16 v132, v132, v132, -2.0 op_sel:[0,1,1] op_sel_hi:[1,1,0]
	ds_read_b128 v[152:155], v234 offset:8192
	ds_read_b128 v[156:159], v234 offset:9216
	ds_read_b128 v[164:167], v234 offset:10240
	ds_read_b128 v[168:171], v234 offset:11264
	ds_read_b128 v[236:239], v234 offset:12288
	ds_read_b128 v[240:243], v234 offset:13312
	v_cvt_scalef32_pk_fp8_f16 v130, v132, 1.0
	v_pk_fma_f16 v132, v132, v132, -2.0 op_sel:[0,1,1] op_sel_hi:[1,1,0]
	v_mul_f32_e32 v135, 0.15915494, v163
	s_waitcnt lgkmcnt(4)
	v_mfma_scale_f32_32x32x64_f8f6f4 v[96:111], v[152:159], v[136:143], v[96:111], v227, v226 op_sel_hi:[0,0,0]
	v_cvt_scalef32_pk_fp8_f16 v131, v133, 1.0 op_sel:[0,0,1]
	v_pk_fma_f16 v133, v133, v133, -2.0 op_sel:[0,1,1] op_sel_hi:[1,1,0]
	v_cvt_scalef32_pk_fp8_f16 v130, v132, 1.0 op_sel:[0,0,1]
	v_cvt_scalef32_pk_fp8_f16 v132, v133, 1.0
	v_pk_fma_f16 v133, v133, v133, -2.0 op_sel:[0,1,1] op_sel_hi:[1,1,0]
	ds_read_b128 v[244:247], v234 offset:14336
	ds_read_b128 v[248:251], v234 offset:15360
	v_pk_fma_f16 v134, v133, v133, -2.0 op_sel:[0,1,1] op_sel_hi:[1,1,0]
	v_cvt_scalef32_pk_fp8_f16 v132, v133, 1.0 op_sel:[0,0,1]
	v_cvt_scalef32_pk_fp8_f16 v133, v134, 1.0
	v_pk_fma_f16 v134, v134, v134, -2.0 op_sel:[0,1,1] op_sel_hi:[1,1,0]
	s_nop 0
	v_cvt_scalef32_pk_fp8_f16 v133, v134, 1.0 op_sel:[0,0,1]
	v_mfma_scale_f32_32x32x64_f8f6f4 v[112:127], v[152:159], v[144:151], v[112:127], v227, v226 op_sel_hi:[0,0,0]
	v_cos_f32_e32 v152, v135
	v_sin_f32_e32 v135, v135
	v_mul_f32_e32 v154, 0.15915494, v194
	v_cos_f32_e32 v155, v154
	v_add_f32_e32 v134, v152, v152
	v_cvt_pk_f16_f32 v152, v135, v134
	v_pk_fma_f16 v153, v152, v152, -2.0 op_sel:[1,0,1] op_sel_hi:[1,1,0]
	v_sin_f32_e32 v154, v154
	v_pk_fma_f16 v134, v153, v153, -2.0 op_sel:[0,1,1] op_sel_hi:[1,1,0]
	s_nop 0
	v_pk_fma_f16 v160, v134, v134, -2.0 op_sel:[0,1,1] op_sel_hi:[1,1,0]
	v_cvt_scalef32_pk_fp8_f16 v135, v134, 1.0
	v_cvt_scalef32_pk_fp8_f16 v134, v152, 1.0
	v_add_f32_e32 v152, v155, v155
	s_waitcnt lgkmcnt(4)
	v_mfma_scale_f32_32x32x64_f8f6f4 v[64:79], v[164:171], v[136:143], v[64:79], v227, v226 op_sel_hi:[0,0,0]
	v_mul_f32_e32 v157, 0.15915494, v195
	v_cvt_pk_f16_f32 v154, v154, v152
	v_cos_f32_e32 v158, v157
	v_pk_fma_f16 v155, v154, v154, -2.0 op_sel:[1,0,1] op_sel_hi:[1,1,0]
	v_sin_f32_e32 v157, v157
	v_pk_fma_f16 v152, v155, v155, -2.0 op_sel:[0,1,1] op_sel_hi:[1,1,0]
	v_cvt_scalef32_pk_fp8_f16 v134, v153, 1.0 op_sel:[0,0,1]
	v_pk_fma_f16 v156, v152, v152, -2.0 op_sel:[0,1,1] op_sel_hi:[1,1,0]
	v_cvt_scalef32_pk_fp8_f16 v153, v152, 1.0
	v_cvt_scalef32_pk_fp8_f16 v152, v154, 1.0
	v_add_f32_e32 v154, v158, v158
	v_mul_f32_e32 v159, 0.15915494, v196
	v_cvt_scalef32_pk_fp8_f16 v152, v155, 1.0 op_sel:[0,0,1]
	v_mfma_scale_f32_32x32x64_f8f6f4 v[80:95], v[164:171], v[144:151], v[80:95], v227, v226 op_sel_hi:[0,0,0]
	v_cvt_pk_f16_f32 v154, v157, v154
	v_cvt_scalef32_pk_fp8_f16 v153, v156, 1.0 op_sel:[0,0,1]
	v_cvt_scalef32_pk_fp8_f16 v155, v154, 1.0
	v_pk_fma_f16 v156, v156, v156, -2.0 op_sel:[0,1,1] op_sel_hi:[1,1,0]
	v_pk_fma_f16 v157, v154, v154, -2.0 op_sel:[1,0,1] op_sel_hi:[1,1,0]
	v_cvt_scalef32_pk_fp8_f16 v154, v156, 1.0
	v_pk_fma_f16 v156, v156, v156, -2.0 op_sel:[0,1,1] op_sel_hi:[1,1,0]
	v_cvt_scalef32_pk_fp8_f16 v155, v157, 1.0 op_sel:[0,0,1]
	v_pk_fma_f16 v157, v157, v157, -2.0 op_sel:[0,1,1] op_sel_hi:[1,1,0]
	v_cvt_scalef32_pk_fp8_f16 v154, v156, 1.0 op_sel:[0,0,1]
	v_cvt_scalef32_pk_fp8_f16 v156, v157, 1.0
	v_pk_fma_f16 v157, v157, v157, -2.0 op_sel:[0,1,1] op_sel_hi:[1,1,0]
	s_waitcnt lgkmcnt(0)
	v_mfma_scale_f32_32x32x64_f8f6f4 v[0:15], v[244:251], v[136:143], v[0:15], v227, v226 op_sel_hi:[0,0,0]
	v_cvt_scalef32_pk_fp8_f16 v156, v157, 1.0 op_sel:[0,0,1]
	v_pk_fma_f16 v158, v157, v157, -2.0 op_sel:[0,1,1] op_sel_hi:[1,1,0]
	v_cvt_scalef32_pk_fp8_f16 v135, v160, 1.0 op_sel:[0,0,1]
	v_cvt_scalef32_pk_fp8_f16 v157, v158, 1.0
	v_mfma_scale_f32_32x32x64_f8f6f4 v[32:47], v[236:243], v[136:143], v[32:47], v227, v226 op_sel_hi:[0,0,0]
	v_cos_f32_e32 v136, v159
	v_sin_f32_e32 v137, v159
	v_pk_fma_f16 v138, v158, v158, -2.0 op_sel:[0,1,1] op_sel_hi:[1,1,0]
	v_add_f32_e32 v136, v136, v136
	v_cvt_pk_f16_f32 v136, v137, v136
	v_pk_fma_f16 v137, v136, v136, -2.0 op_sel:[1,0,1] op_sel_hi:[1,1,0]
	v_cvt_scalef32_pk_fp8_f16 v157, v138, 1.0 op_sel:[0,0,1]
	v_pk_fma_f16 v138, v137, v137, -2.0 op_sel:[0,1,1] op_sel_hi:[1,1,0]
	s_nop 0
	v_pk_fma_f16 v180, v138, v138, -2.0 op_sel:[0,1,1] op_sel_hi:[1,1,0]
	v_cvt_scalef32_pk_fp8_f16 v159, v138, 1.0
	v_cvt_scalef32_pk_fp8_f16 v158, v136, 1.0
	v_cvt_scalef32_pk_fp8_f16 v159, v180, 1.0 op_sel:[0,0,1]
	v_cvt_scalef32_pk_fp8_f16 v158, v137, 1.0 op_sel:[0,0,1]
	v_mfma_scale_f32_32x32x64_f8f6f4 v[48:63], v[236:243], v[144:151], v[48:63], v227, v226 op_sel_hi:[0,0,0]
	v_mfma_scale_f32_32x32x64_f8f6f4 v[16:31], v[244:251], v[144:151], v[16:31], v227, v226 op_sel_hi:[0,0,0]
	ds_read_b128 v[140:143], v234 offset:16384
	ds_read_b128 v[144:147], v234 offset:17408
	ds_read_b128 v[236:239], v234 offset:18432
	ds_read_b128 v[240:243], v234 offset:19456
	ds_read_b128 v[170:173], v234 offset:20480
	ds_read_b128 v[174:177], v234 offset:21504
	s_waitcnt lgkmcnt(4)
	v_mfma_scale_f32_32x32x64_f8f6f4 v[96:111], v[140:147], v[128:135], v[96:111], v227, v226 op_sel_hi:[0,0,0]
	v_pk_fma_f16 v139, v160, v160, -2.0 op_sel:[0,1,1] op_sel_hi:[1,1,0]
	v_mov_b32_e32 v160, v204
	ds_read_b128 v[162:165], v234 offset:22528
	ds_read_b128 v[166:169], v234 offset:23552
	v_mul_f32_e32 v136, 0.15915494, v201
	v_cos_f32_e32 v137, v136
	v_sin_f32_e32 v136, v136
	v_mul_f32_e32 v150, 0.15915494, v186
	v_cos_f32_e32 v151, v150
	v_add_f32_e32 v137, v137, v137
	v_cvt_pk_f16_f32 v136, v136, v137
	v_pk_fma_f16 v138, v136, v136, -2.0 op_sel:[1,0,1] op_sel_hi:[1,1,0]
	v_cvt_scalef32_pk_fp8_f16 v137, v136, 1.0
	v_mfma_scale_f32_32x32x64_f8f6f4 v[112:127], v[140:147], v[152:159], v[112:127], v227, v226 op_sel_hi:[0,0,0]
	v_mul_f32_e32 v140, 0.15915494, v178
	v_cos_f32_e32 v141, v140
	v_sin_f32_e32 v140, v140
	v_mul_f32_e32 v143, 0.15915494, v200
	v_cos_f32_e32 v144, v143
	v_add_f32_e32 v141, v141, v141
	v_cvt_pk_f16_f32 v141, v140, v141
	v_sin_f32_e32 v143, v143
	v_cvt_scalef32_pk_fp8_f16 v140, v141, 1.0
	v_pk_fma_f16 v141, v141, v141, -2.0 op_sel:[1,0,1] op_sel_hi:[1,1,0]
	v_mul_f32_e32 v146, 0.15915494, v197
	v_pk_fma_f16 v142, v141, v141, -2.0 op_sel:[0,1,1] op_sel_hi:[1,1,0]
	v_cvt_scalef32_pk_fp8_f16 v140, v141, 1.0 op_sel:[0,0,1]
	v_cvt_scalef32_pk_fp8_f16 v141, v142, 1.0
	v_pk_fma_f16 v145, v142, v142, -2.0 op_sel:[0,1,1] op_sel_hi:[1,1,0]
	v_add_f32_e32 v142, v144, v144
	v_cvt_pk_f16_f32 v144, v143, v142
	v_lshl_add_u64 v[142:143], v[160:161], 2, s[4:5]
	global_load_dwordx4 v[198:201], v[142:143], off offset:16
	global_load_dwordx4 v[194:197], v[142:143], off offset:3472
	v_cvt_scalef32_pk_fp8_f16 v141, v145, 1.0 op_sel:[0,0,1]
	v_pk_fma_f16 v160, v144, v144, -2.0 op_sel:[1,0,1] op_sel_hi:[1,1,0]
	v_cvt_scalef32_pk_fp8_f16 v143, v144, 1.0
	v_pk_fma_f16 v144, v145, v145, -2.0 op_sel:[0,1,1] op_sel_hi:[1,1,0]
	v_cos_f32_e32 v145, v146
	v_sin_f32_e32 v146, v146
	v_pk_fma_f16 v148, v138, v138, -2.0 op_sel:[0,1,1] op_sel_hi:[1,1,0]
	v_cvt_scalef32_pk_fp8_f16 v136, v139, 1.0
	v_pk_fma_f16 v139, v139, v139, -2.0 op_sel:[0,1,1] op_sel_hi:[1,1,0]
	v_pk_fma_f16 v149, v148, v148, -2.0 op_sel:[0,1,1] op_sel_hi:[1,1,0]
	v_cvt_scalef32_pk_fp8_f16 v142, v144, 1.0
	v_pk_fma_f16 v144, v144, v144, -2.0 op_sel:[0,1,1] op_sel_hi:[1,1,0]
	v_cvt_scalef32_pk_fp8_f16 v137, v138, 1.0 op_sel:[0,0,1]
	v_cvt_scalef32_pk_fp8_f16 v136, v139, 1.0 op_sel:[0,0,1]
	v_pk_fma_f16 v138, v149, v149, -2.0 op_sel:[0,1,1] op_sel_hi:[1,1,0]
	v_cvt_scalef32_pk_fp8_f16 v142, v144, 1.0 op_sel:[0,0,1]
	v_add_f32_e32 v144, v145, v145
	v_cvt_scalef32_pk_fp8_f16 v139, v138, 1.0
	v_pk_fma_f16 v138, v138, v138, -2.0 op_sel:[0,1,1] op_sel_hi:[1,1,0]
	s_waitcnt lgkmcnt(4)
	v_mfma_scale_f32_32x32x64_f8f6f4 v[64:79], v[236:243], v[128:135], v[64:79], v227, v226 op_sel_hi:[0,0,0]
	v_cvt_pk_f16_f32 v144, v146, v144
	v_cvt_scalef32_pk_fp8_f16 v139, v138, 1.0 op_sel:[0,0,1]
	v_pk_fma_f16 v146, v144, v144, -2.0 op_sel:[1,0,1] op_sel_hi:[1,1,0]
	v_cvt_scalef32_pk_fp8_f16 v138, v148, 1.0
	v_cvt_scalef32_pk_fp8_f16 v145, v144, 1.0
	v_pk_fma_f16 v147, v180, v180, -2.0 op_sel:[0,1,1] op_sel_hi:[1,1,0]
	v_pk_fma_f16 v148, v146, v146, -2.0 op_sel:[0,1,1] op_sel_hi:[1,1,0]
	v_cvt_scalef32_pk_fp8_f16 v138, v149, 1.0 op_sel:[0,0,1]
	v_cvt_scalef32_pk_fp8_f16 v144, v147, 1.0
	v_pk_fma_f16 v147, v147, v147, -2.0 op_sel:[0,1,1] op_sel_hi:[1,1,0]
	v_pk_fma_f16 v149, v148, v148, -2.0 op_sel:[0,1,1] op_sel_hi:[1,1,0]
	v_cvt_scalef32_pk_fp8_f16 v145, v146, 1.0 op_sel:[0,0,1]
	v_mfma_scale_f32_32x32x64_f8f6f4 v[80:95], v[236:243], v[152:159], v[80:95], v227, v226 op_sel_hi:[0,0,0]
	v_pk_fma_f16 v146, v149, v149, -2.0 op_sel:[0,1,1] op_sel_hi:[1,1,0]
	v_cvt_scalef32_pk_fp8_f16 v144, v147, 1.0 op_sel:[0,0,1]
	v_cvt_scalef32_pk_fp8_f16 v147, v146, 1.0
	v_pk_fma_f16 v146, v146, v146, -2.0 op_sel:[0,1,1] op_sel_hi:[1,1,0]
	v_sin_f32_e32 v150, v150
	v_cvt_scalef32_pk_fp8_f16 v147, v146, 1.0 op_sel:[0,0,1]
	v_cvt_scalef32_pk_fp8_f16 v146, v148, 1.0
	v_add_f32_e32 v148, v151, v151
	v_mul_f32_e32 v151, 0.15915494, v187
	v_cvt_scalef32_pk_fp8_f16 v146, v149, 1.0 op_sel:[0,0,1]
	v_cvt_pk_f16_f32 v149, v150, v148
	v_cvt_scalef32_pk_fp8_f16 v148, v149, 1.0
	s_waitcnt lgkmcnt(0)
	v_mfma_scale_f32_32x32x64_f8f6f4 v[0:15], v[162:169], v[128:135], v[0:15], v227, v226 op_sel_hi:[0,0,0]
	v_pk_fma_f16 v149, v149, v149, -2.0 op_sel:[1,0,1] op_sel_hi:[1,1,0]
	v_cvt_scalef32_pk_fp8_f16 v143, v160, 1.0 op_sel:[0,0,1]
	v_pk_fma_f16 v150, v149, v149, -2.0 op_sel:[0,1,1] op_sel_hi:[1,1,0]
	v_cvt_scalef32_pk_fp8_f16 v148, v149, 1.0 op_sel:[0,0,1]
	v_cvt_scalef32_pk_fp8_f16 v149, v150, 1.0
	v_mfma_scale_f32_32x32x64_f8f6f4 v[32:47], v[170:177], v[128:135], v[32:47], v227, v226 op_sel_hi:[0,0,0]
	v_cos_f32_e32 v128, v151
	v_sin_f32_e32 v129, v151
	v_pk_fma_f16 v130, v150, v150, -2.0 op_sel:[0,1,1] op_sel_hi:[1,1,0]
	v_add_f32_e32 v128, v128, v128
	v_cvt_pk_f16_f32 v128, v129, v128
	v_pk_fma_f16 v203, v128, v128, -2.0 op_sel:[1,0,1] op_sel_hi:[1,1,0]
	v_cvt_scalef32_pk_fp8_f16 v151, v128, 1.0
	v_pk_fma_f16 v128, v130, v130, -2.0 op_sel:[0,1,1] op_sel_hi:[1,1,0]
	s_nop 0
	v_cvt_scalef32_pk_fp8_f16 v150, v128, 1.0
	v_pk_fma_f16 v128, v128, v128, -2.0 op_sel:[0,1,1] op_sel_hi:[1,1,0]
	v_cvt_scalef32_pk_fp8_f16 v149, v130, 1.0 op_sel:[0,0,1]
	v_cvt_scalef32_pk_fp8_f16 v151, v203, 1.0 op_sel:[0,0,1]
	v_cvt_scalef32_pk_fp8_f16 v150, v128, 1.0 op_sel:[0,0,1]
	v_mfma_scale_f32_32x32x64_f8f6f4 v[48:63], v[170:177], v[152:159], v[48:63], v227, v226 op_sel_hi:[0,0,0]
	v_mfma_scale_f32_32x32x64_f8f6f4 v[16:31], v[162:169], v[152:159], v[16:31], v227, v226 op_sel_hi:[0,0,0]
	v_pk_fma_f16 v130, v160, v160, -2.0 op_sel:[0,1,1] op_sel_hi:[1,1,0]
	s_nop 0
	v_pk_fma_f16 v131, v130, v130, -2.0 op_sel:[0,1,1] op_sel_hi:[1,1,0]
	ds_read_b128 v[152:155], v234 offset:24576
	ds_read_b128 v[156:159], v234 offset:25600
	ds_read_b128 v[162:165], v234 offset:26624
	ds_read_b128 v[166:169], v234 offset:27648
	v_pk_fma_f16 v128, v131, v131, -2.0 op_sel:[0,1,1] op_sel_hi:[1,1,0]
	v_mov_b32_e32 v160, v204
	v_pk_fma_f16 v132, v128, v128, -2.0 op_sel:[0,1,1] op_sel_hi:[1,1,0]
	v_cvt_scalef32_pk_fp8_f16 v129, v128, 1.0
	v_cvt_scalef32_pk_fp8_f16 v129, v132, 1.0 op_sel:[0,0,1]
	v_mul_f32_e32 v132, 0.15915494, v179
	v_sin_f32_e32 v133, v132
	v_cos_f32_e32 v132, v132
	v_cvt_scalef32_pk_fp8_f16 v128, v130, 1.0
	v_cvt_scalef32_pk_fp8_f16 v128, v131, 1.0 op_sel:[0,0,1]
	v_add_f32_e32 v130, v132, v132
	v_cvt_pk_f16_f32 v132, v133, v130
	v_pk_fma_f16 v133, v132, v132, -2.0 op_sel:[1,0,1] op_sel_hi:[1,1,0]
	s_nop 0
	v_pk_fma_f16 v130, v133, v133, -2.0 op_sel:[0,1,1] op_sel_hi:[1,1,0]
	s_waitcnt lgkmcnt(2)
	v_mfma_scale_f32_32x32x64_f8f6f4 v[96:111], v[152:159], v[136:143], v[96:111], v227, v226 op_sel_hi:[0,0,0]
	v_cvt_scalef32_pk_fp8_f16 v131, v130, 1.0
	v_pk_fma_f16 v134, v130, v130, -2.0 op_sel:[0,1,1] op_sel_hi:[1,1,0]
	v_cvt_scalef32_pk_fp8_f16 v130, v132, 1.0
	v_cvt_scalef32_pk_fp8_f16 v131, v134, 1.0 op_sel:[0,0,1]
	v_cvt_scalef32_pk_fp8_f16 v130, v133, 1.0 op_sel:[0,0,1]
	v_pk_fma_f16 v133, v134, v134, -2.0 op_sel:[0,1,1] op_sel_hi:[1,1,0]
	v_mul_f32_e32 v134, 0.15915494, v181
	v_cos_f32_e32 v135, v134
	v_sin_f32_e32 v134, v134
	v_cvt_scalef32_pk_fp8_f16 v132, v133, 1.0
	v_pk_fma_f16 v133, v133, v133, -2.0 op_sel:[0,1,1] op_sel_hi:[1,1,0]
	ds_read_b128 v[170:173], v234 offset:28672
	ds_read_b128 v[174:177], v234 offset:29696
	ds_read_b128 v[236:239], v234 offset:30720
	ds_read_b128 v[240:243], v234 offset:31744
	v_cvt_scalef32_pk_fp8_f16 v132, v133, 1.0 op_sel:[0,0,1]
	v_add_f32_e32 v133, v135, v135
	v_mfma_scale_f32_32x32x64_f8f6f4 v[112:127], v[152:159], v[144:151], v[112:127], v227, v226 op_sel_hi:[0,0,0]
	v_cvt_pk_f16_f32 v152, v134, v133
	v_mul_f32_e32 v153, 0.15915494, v188
	v_lshl_add_u64 v[134:135], v[160:161], 2, s[4:5]
	v_mul_f32_e32 v154, 0.15915494, v189
	global_load_dwordx4 v[178:181], v[134:135], off offset:32
	global_load_dwordx4 v[186:189], v[134:135], off offset:3488
	v_pk_fma_f16 v134, v152, v152, -2.0 op_sel:[1,0,1] op_sel_hi:[1,1,0]
	v_cvt_scalef32_pk_fp8_f16 v133, v152, 1.0
	v_pk_fma_f16 v152, v134, v134, -2.0 op_sel:[0,1,1] op_sel_hi:[1,1,0]
	v_cvt_scalef32_pk_fp8_f16 v133, v134, 1.0 op_sel:[0,0,1]
	v_pk_fma_f16 v155, v152, v152, -2.0 op_sel:[0,1,1] op_sel_hi:[1,1,0]
	s_nop 0
	v_pk_fma_f16 v134, v155, v155, -2.0 op_sel:[0,1,1] op_sel_hi:[1,1,0]
	s_nop 0
	v_pk_fma_f16 v156, v134, v134, -2.0 op_sel:[0,1,1] op_sel_hi:[1,1,0]
	v_cvt_scalef32_pk_fp8_f16 v135, v134, 1.0
	v_cvt_scalef32_pk_fp8_f16 v134, v152, 1.0
	v_pk_fma_f16 v152, v203, v203, -2.0 op_sel:[0,1,1] op_sel_hi:[1,1,0]
	v_cvt_scalef32_pk_fp8_f16 v134, v155, 1.0 op_sel:[0,0,1]
	v_pk_fma_f16 v155, v152, v152, -2.0 op_sel:[0,1,1] op_sel_hi:[1,1,0]
	s_waitcnt lgkmcnt(4)
	v_mfma_scale_f32_32x32x64_f8f6f4 v[64:79], v[162:169], v[136:143], v[64:79], v227, v226 op_sel_hi:[0,0,0]
	v_cvt_scalef32_pk_fp8_f16 v135, v156, 1.0 op_sel:[0,0,1]
	v_pk_fma_f16 v156, v155, v155, -2.0 op_sel:[0,1,1] op_sel_hi:[1,1,0]
	s_nop 0
	v_pk_fma_f16 v157, v156, v156, -2.0 op_sel:[0,1,1] op_sel_hi:[1,1,0]
	v_mfma_scale_f32_32x32x64_f8f6f4 v[80:95], v[162:169], v[144:151], v[80:95], v227, v226 op_sel_hi:[0,0,0]
	v_cvt_scalef32_pk_fp8_f16 v165, v156, 1.0
	v_cos_f32_e32 v156, v153
	v_sin_f32_e32 v153, v153
	v_cvt_scalef32_pk_fp8_f16 v164, v152, 1.0
	v_add_f32_e32 v152, v156, v156
	v_cvt_pk_f16_f32 v152, v153, v152
	v_pk_fma_f16 v153, v152, v152, -2.0 op_sel:[1,0,1] op_sel_hi:[1,1,0]
	v_cvt_scalef32_pk_fp8_f16 v166, v152, 1.0
	v_cvt_scalef32_pk_fp8_f16 v164, v155, 1.0 op_sel:[0,0,1]
	v_pk_fma_f16 v155, v153, v153, -2.0 op_sel:[0,1,1] op_sel_hi:[1,1,0]
	v_cvt_scalef32_pk_fp8_f16 v166, v153, 1.0 op_sel:[0,0,1]
	s_waitcnt lgkmcnt(0)
	v_mfma_scale_f32_32x32x64_f8f6f4 v[0:15], v[236:243], v[136:143], v[0:15], v227, v226 op_sel_hi:[0,0,0]
	v_cos_f32_e32 v153, v154
	v_cvt_scalef32_pk_fp8_f16 v167, v155, 1.0
	v_pk_fma_f16 v155, v155, v155, -2.0 op_sel:[0,1,1] op_sel_hi:[1,1,0]
	v_sin_f32_e32 v154, v154
	v_pk_fma_f16 v152, v155, v155, -2.0 op_sel:[0,1,1] op_sel_hi:[1,1,0]
	s_nop 0
	v_cvt_scalef32_pk_fp8_f16 v168, v152, 1.0
	v_pk_fma_f16 v152, v152, v152, -2.0 op_sel:[0,1,1] op_sel_hi:[1,1,0]
	s_nop 0
	v_cvt_scalef32_pk_fp8_f16 v168, v152, 1.0 op_sel:[0,0,1]
	v_add_f32_e32 v152, v153, v153
	v_cvt_scalef32_pk_fp8_f16 v165, v157, 1.0 op_sel:[0,0,1]
	v_cvt_scalef32_pk_fp8_f16 v167, v155, 1.0 op_sel:[0,0,1]
	v_mfma_scale_f32_32x32x64_f8f6f4 v[32:47], v[170:177], v[136:143], v[32:47], v227, v226 op_sel_hi:[0,0,0]
	v_cvt_pk_f16_f32 v136, v154, v152
	v_cvt_scalef32_pk_fp8_f16 v169, v136, 1.0
	v_pk_fma_f16 v136, v136, v136, -2.0 op_sel:[1,0,1] op_sel_hi:[1,1,0]
	s_nop 0
	v_cvt_scalef32_pk_fp8_f16 v169, v136, 1.0 op_sel:[0,0,1]
	v_pk_fma_f16 v136, v136, v136, -2.0 op_sel:[0,1,1] op_sel_hi:[1,1,0]
	s_nop 0
	v_pk_fma_f16 v137, v136, v136, -2.0 op_sel:[0,1,1] op_sel_hi:[1,1,0]
	s_nop 0
	v_pk_fma_f16 v138, v137, v137, -2.0 op_sel:[0,1,1] op_sel_hi:[1,1,0]
	s_nop 0
	v_pk_fma_f16 v139, v138, v138, -2.0 op_sel:[0,1,1] op_sel_hi:[1,1,0]
	v_mfma_scale_f32_32x32x64_f8f6f4 v[48:63], v[170:177], v[144:151], v[48:63], v227, v226 op_sel_hi:[0,0,0]
	v_cvt_scalef32_pk_fp8_f16 v171, v138, 1.0
	v_cvt_scalef32_pk_fp8_f16 v170, v136, 1.0
	v_cvt_scalef32_pk_fp8_f16 v171, v139, 1.0 op_sel:[0,0,1]
	v_cvt_scalef32_pk_fp8_f16 v170, v137, 1.0 op_sel:[0,0,1]
	v_mfma_scale_f32_32x32x64_f8f6f4 v[16:31], v[236:243], v[144:151], v[16:31], v227, v226 op_sel_hi:[0,0,0]
	v_mul_f32_e32 v152, 0.15915494, v225
	ds_read_b128 v[136:139], v234 offset:32768
	ds_read_b128 v[140:143], v234 offset:33792
	v_cos_f32_e32 v153, v152
	v_sin_f32_e32 v152, v152
	v_mov_b32_e32 v205, v161
	s_waitcnt lgkmcnt(0)
	v_mfma_scale_f32_32x32x64_f8f6f4 v[96:111], v[136:143], v[128:135], v[96:111], v227, v226 op_sel_hi:[0,0,0]
	v_add_f32_e32 v153, v153, v153
	v_cvt_pk_f16_f32 v158, v152, v153
	v_mov_b32_e32 v203, v161
	v_cndmask_b32_e64 v162, 0, v222, s[0:1]
	v_mul_f32_e32 v163, 0.15915494, v223
	v_pk_fma_f16 v159, v158, v158, -2.0 op_sel:[1,0,1] op_sel_hi:[1,1,0]
	v_cndmask_b32_e64 v172, 0, v224, s[0:1]
	v_pk_fma_f16 v156, v159, v159, -2.0 op_sel:[0,1,1] op_sel_hi:[1,1,0]
	s_nop 0
	v_pk_fma_f16 v160, v156, v156, -2.0 op_sel:[0,1,1] op_sel_hi:[1,1,0]
	v_cvt_scalef32_pk_fp8_f16 v157, v156, 1.0
	v_cvt_scalef32_pk_fp8_f16 v156, v158, 1.0
	v_cvt_scalef32_pk_fp8_f16 v156, v159, 1.0 op_sel:[0,0,1]
	v_mfma_scale_f32_32x32x64_f8f6f4 v[112:127], v[136:143], v[164:171], v[112:127], v227, v226 op_sel_hi:[0,0,0]
	ds_read_b128 v[136:139], v234 offset:34816
	ds_read_b128 v[140:143], v234 offset:35840
	ds_read_b128 v[144:147], v234 offset:36864
	ds_read_b128 v[148:151], v234 offset:37888
	ds_read_b128 v[236:239], v234 offset:38912
	ds_read_b128 v[240:243], v234 offset:39936
	v_lshl_add_u64 v[152:153], v[204:205], 2, s[4:5]
	v_lshl_add_u64 v[154:155], v[202:203], 2, s[4:5]
	global_load_dword v225, v[152:153], off offset:48
	global_load_dword v222, v[154:155], off
	global_load_dword v224, v[154:155], off offset:3456
	global_load_dword v223, v[152:153], off offset:3504
	v_cvt_scalef32_pk_fp8_f16 v157, v160, 1.0 op_sel:[0,0,1]
	s_waitcnt lgkmcnt(4)
	v_mfma_scale_f32_32x32x64_f8f6f4 v[64:79], v[136:143], v[128:135], v[64:79], v227, v226 op_sel_hi:[0,0,0]
	v_mfma_scale_f32_32x32x64_f8f6f4 v[80:95], v[136:143], v[164:171], v[80:95], v227, v226 op_sel_hi:[0,0,0]
	v_mul_f32_e32 v136, v207, v208
	v_fma_f32 v137, v208, v208, -2.0
	v_cndmask_b32_e64 v138, v137, v136, s[0:1]
	v_mul_f32_e32 v136, v136, v137
	v_fma_f32 v137, v137, v137, -2.0
	v_cndmask_b32_e64 v139, v137, v136, s[0:1]
	v_cvt_pk_fp8_f32 v159, v138, v139
	v_mul_f32_e32 v136, v136, v137
	v_fma_f32 v137, v137, v137, -2.0
	v_cndmask_b32_e64 v136, v137, v136, s[0:1]
	v_cvt_pk_fp8_f32 v159, v136, v162 op_sel:[0,0,1]
	v_pk_fma_f16 v136, v160, v160, -2.0 op_sel:[0,1,1] op_sel_hi:[1,1,0]
	v_mov_b32_e32 v160, v161
	v_pk_fma_f16 v137, v136, v136, -2.0 op_sel:[0,1,1] op_sel_hi:[1,1,0]
	v_cvt_scalef32_pk_fp8_f16 v158, v136, 1.0
	v_cos_f32_e32 v136, v163
	v_cvt_scalef32_pk_fp8_f16 v158, v137, 1.0 op_sel:[0,0,1]
	v_sin_f32_e32 v137, v163
	s_waitcnt lgkmcnt(0)
	v_mfma_scale_f32_32x32x64_f8f6f4 v[0:15], v[236:243], v[128:135], v[0:15], v227, v226 op_sel_hi:[0,0,0]
	v_add_f32_e32 v136, v136, v136
	v_mov_b32_e32 v162, v161
	v_cvt_pk_f16_f32 v138, v137, v136
	v_pk_fma_f16 v139, v138, v138, -2.0 op_sel:[1,0,1] op_sel_hi:[1,1,0]
	s_nop 0
	v_pk_fma_f16 v136, v139, v139, -2.0 op_sel:[0,1,1] op_sel_hi:[1,1,0]
	v_mov_b32_e32 v163, v161
	v_pk_fma_f16 v140, v136, v136, -2.0 op_sel:[0,1,1] op_sel_hi:[1,1,0]
	v_cvt_scalef32_pk_fp8_f16 v137, v136, 1.0
	v_cvt_scalef32_pk_fp8_f16 v136, v138, 1.0
	v_cvt_scalef32_pk_fp8_f16 v136, v139, 1.0 op_sel:[0,0,1]
	v_mul_f32_e32 v138, v209, v210
	v_fma_f32 v139, v210, v210, -2.0
	v_cndmask_b32_e64 v141, v139, v138, s[0:1]
	v_mul_f32_e32 v138, v138, v139
	v_fma_f32 v142, v139, v139, -2.0
	v_cndmask_b32_e64 v143, v142, v138, s[0:1]
	v_cvt_pk_fp8_f32 v139, v141, v143
	v_mfma_scale_f32_32x32x64_f8f6f4 v[32:47], v[144:151], v[128:135], v[32:47], v227, v226 op_sel_hi:[0,0,0]
	v_mul_f32_e32 v128, v138, v142
	v_fma_f32 v129, v142, v142, -2.0
	v_cndmask_b32_e64 v128, v129, v128, s[0:1]
	v_cvt_pk_fp8_f32 v139, v128, v172 op_sel:[0,0,1]
	v_pk_fma_f16 v128, v140, v140, -2.0 op_sel:[0,1,1] op_sel_hi:[1,1,0]
	s_nop 0
	v_cvt_scalef32_pk_fp8_f16 v138, v128, 1.0
	v_pk_fma_f16 v128, v128, v128, -2.0 op_sel:[0,1,1] op_sel_hi:[1,1,0]
	v_cvt_scalef32_pk_fp8_f16 v137, v140, 1.0 op_sel:[0,0,1]
	v_cvt_scalef32_pk_fp8_f16 v138, v128, 1.0 op_sel:[0,0,1]
	v_mov_b32_e32 v140, v161
	v_mov_b32_e32 v141, v161
	v_mov_b32_e32 v142, v161
	v_mov_b32_e32 v143, v161
	v_mfma_scale_f32_32x32x64_f8f6f4 v[48:63], v[144:151], v[164:171], v[48:63], v227, v226 op_sel_hi:[0,0,0]
	v_mfma_scale_f32_32x32x64_f8f6f4 v[16:31], v[236:243], v[164:171], v[16:31], v227, v226 op_sel_hi:[0,0,0]
	ds_read_b128 v[128:131], v234 offset:40960
	ds_read_b128 v[132:135], v234 offset:41984
	s_waitcnt lgkmcnt(0)
	v_mfma_scale_f32_32x32x64_f8f6f4 v[96:111], v[128:135], v[156:163], v[96:111], v227, v226 op_sel_hi:[0,0,0]
	v_mfma_scale_f32_32x32x64_f8f6f4 v[112:127], v[128:135], v[136:143], v[112:127], v227, v226 op_sel_hi:[0,0,0]
	ds_read_b128 v[128:131], v234 offset:43008
	ds_read_b128 v[132:135], v234 offset:44032
	s_waitcnt lgkmcnt(0)
	v_mfma_scale_f32_32x32x64_f8f6f4 v[64:79], v[128:135], v[156:163], v[64:79], v227, v226 op_sel_hi:[0,0,0]
	v_mfma_scale_f32_32x32x64_f8f6f4 v[80:95], v[128:135], v[136:143], v[80:95], v227, v226 op_sel_hi:[0,0,0]
	ds_read_b128 v[128:131], v234 offset:45056
	ds_read_b128 v[132:135], v234 offset:46080
	s_waitcnt lgkmcnt(0)
	v_mfma_scale_f32_32x32x64_f8f6f4 v[32:47], v[128:135], v[156:163], v[32:47], v227, v226 op_sel_hi:[0,0,0]
	v_mfma_scale_f32_32x32x64_f8f6f4 v[48:63], v[128:135], v[136:143], v[48:63], v227, v226 op_sel_hi:[0,0,0]
	ds_read_b128 v[128:131], v234 offset:47104
	ds_read_b128 v[132:135], v234 offset:48128
	ds_read_b128 v[174:177], v234 offset:49152
	ds_read_b128 v[208:211], v234 offset:50176
	ds_read_b128 v[212:215], v234 offset:53248
	ds_read_b128 v[236:239], v234 offset:54272
	s_waitcnt lgkmcnt(4)
	v_mfma_scale_f32_32x32x64_f8f6f4 v[0:15], v[128:135], v[156:163], v[0:15], v227, v226 op_sel_hi:[0,0,0]
	v_mfma_scale_f32_32x32x64_f8f6f4 v[16:31], v[128:135], v[136:143], v[16:31], v227, v226 op_sel_hi:[0,0,0]
	v_cvt_pk_bf16_f32 v96, v96, v97
	v_pk_max_i16 v162, v96, 0
	v_cvt_pk_bf16_f32 v96, v98, v99
	v_pk_max_i16 v163, v96, 0
	v_cvt_pk_bf16_f32 v96, v100, v101
	v_pk_max_i16 v164, v96, 0
	v_cvt_pk_bf16_f32 v96, v102, v103
	v_pk_max_i16 v165, v96, 0
	v_cvt_pk_bf16_f32 v96, v112, v113
	v_pk_max_i16 v166, v96, 0
	v_cvt_pk_bf16_f32 v96, v114, v115
	v_pk_max_i16 v167, v96, 0
	v_cvt_pk_bf16_f32 v96, v116, v117
	v_pk_max_i16 v168, v96, 0
	v_cvt_pk_bf16_f32 v96, v118, v119
	v_pk_max_i16 v169, v96, 0
	v_cvt_pk_bf16_f32 v96, v104, v105
	v_pk_max_i16 v170, v96, 0
	v_cvt_pk_bf16_f32 v96, v106, v107
	v_pk_max_i16 v171, v96, 0
	v_cvt_pk_bf16_f32 v96, v108, v109
	v_add_u32_e32 v128, 0, v206
	v_pk_max_i16 v172, v96, 0
	v_cvt_pk_bf16_f32 v96, v110, v111
	v_add_u32_e32 v235, 0x18000, v128
	v_pk_max_i16 v173, v96, 0
	v_cvt_pk_bf16_f32 v96, v120, v121
	ds_read_b128 v[128:131], v235
	ds_read_b128 v[132:135], v235 offset:32
	ds_read_b128 v[136:139], v235 offset:64
	ds_read_b128 v[140:143], v235 offset:96
	v_pk_max_i16 v202, v96, 0
	v_cvt_pk_bf16_f32 v96, v122, v123
	v_pk_max_i16 v203, v96, 0
	ds_read_b128 v[96:99], v235 offset:128
	ds_read_b128 v[100:103], v235 offset:160
	ds_read_b128 v[104:107], v235 offset:192
	ds_read_b128 v[108:111], v235 offset:224
	v_cvt_pk_bf16_f32 v112, v124, v125
	v_cvt_pk_bf16_f32 v64, v64, v65
	s_waitcnt lgkmcnt(4)
	v_mfma_f32_32x32x16_bf16 v[144:159], v[174:177], v[166:169], v[128:143]
	v_pk_max_i16 v204, v112, 0
	v_cvt_pk_bf16_f32 v112, v126, v127
	v_pk_max_i16 v205, v112, 0
	ds_read_b128 v[240:243], v234 offset:57344
	ds_read_b128 v[244:247], v234 offset:58368
	ds_read_b128 v[248:251], v234 offset:61440
	ds_read_b128 v[252:255], v234 offset:62464
	v_cvt_pk_bf16_f32 v65, v74, v75
	v_cndmask_b32_e64 v230, v230, 0, s[14:15]
	v_pk_max_i16 v65, v65, 0
	v_mfma_f32_32x32x16_bf16 v[128:143], v[174:177], v[162:165], v[128:143]
	v_pk_max_i16 v174, v64, 0
	v_cvt_pk_bf16_f32 v64, v66, v67
	v_pk_max_i16 v175, v64, 0
	v_cvt_pk_bf16_f32 v64, v68, v69
	v_pk_max_i16 v176, v64, 0
	v_cvt_pk_bf16_f32 v64, v70, v71
	v_pk_max_i16 v177, v64, 0
	s_waitcnt lgkmcnt(4)
	v_mfma_f32_32x32x16_bf16 v[112:127], v[208:211], v[166:169], v[96:111]
	v_cvt_pk_bf16_f32 v64, v80, v81
	v_pk_max_i16 v80, v64, 0
	v_cvt_pk_bf16_f32 v64, v82, v83
	v_pk_max_i16 v81, v64, 0
	v_cvt_pk_bf16_f32 v64, v84, v85
	v_pk_max_i16 v82, v64, 0
	v_cvt_pk_bf16_f32 v64, v86, v87
	v_mfma_f32_32x32x16_bf16 v[96:111], v[208:211], v[162:165], v[96:111]
	v_pk_max_i16 v83, v64, 0
	v_cvt_pk_bf16_f32 v64, v72, v73
	v_cvt_pk_bf16_f32 v66, v76, v77
	v_pk_max_i16 v64, v64, 0
	v_pk_max_i16 v66, v66, 0
	v_cvt_pk_bf16_f32 v67, v78, v79
	v_cvt_pk_bf16_f32 v68, v88, v89
	v_cvt_pk_bf16_f32 v69, v90, v91
	v_cvt_pk_bf16_f32 v70, v92, v93
	v_cvt_pk_bf16_f32 v71, v94, v95
	v_add_u32_e32 v160, 0x14000, v234
	v_mfma_f32_32x32x16_bf16 v[128:143], v[212:215], v[170:173], v[128:143]
	v_pk_max_i16 v67, v67, 0
	v_pk_max_i16 v68, v68, 0
	v_pk_max_i16 v69, v69, 0
	v_pk_max_i16 v70, v70, 0
	v_pk_max_i16 v71, v71, 0
	v_mfma_f32_32x32x16_bf16 v[144:159], v[212:215], v[202:205], v[144:159]
	v_mfma_f32_32x32x16_bf16 v[96:111], v[236:239], v[170:173], v[96:111]
	v_mfma_f32_32x32x16_bf16 v[112:127], v[236:239], v[202:205], v[112:127]
	v_cvt_pk_bf16_f32 v32, v32, v33
	v_pk_max_i16 v76, v32, 0
	v_cvt_pk_bf16_f32 v32, v34, v35
	v_pk_max_i16 v77, v32, 0
	v_cvt_pk_bf16_f32 v32, v36, v37
	v_pk_max_i16 v78, v32, 0
	v_cvt_pk_bf16_f32 v32, v38, v39
	v_pk_max_i16 v79, v32, 0
	v_cvt_pk_bf16_f32 v32, v48, v49
	v_pk_max_i16 v88, v32, 0
	v_cvt_pk_bf16_f32 v32, v50, v51
	v_pk_max_i16 v89, v32, 0
	v_cvt_pk_bf16_f32 v32, v52, v53
	v_pk_max_i16 v90, v32, 0
	v_cvt_pk_bf16_f32 v32, v54, v55
	s_waitcnt lgkmcnt(3)
	v_mfma_f32_32x32x16_bf16 v[128:143], v[240:243], v[174:177], v[128:143]
	v_pk_max_i16 v91, v32, 0
	v_cvt_pk_bf16_f32 v32, v40, v41
	v_pk_max_i16 v72, v32, 0
	v_cvt_pk_bf16_f32 v32, v42, v43
	v_pk_max_i16 v73, v32, 0
	v_cvt_pk_bf16_f32 v32, v44, v45
	v_pk_max_i16 v74, v32, 0
	v_mfma_f32_32x32x16_bf16 v[144:159], v[240:243], v[80:83], v[144:159]
	ds_read_b128 v[92:95], v233 offset:16384
	ds_read_b128 v[208:211], v233 offset:17408
	ds_read_b128 v[236:239], v233 offset:20480
	ds_read_b128 v[240:243], v233 offset:21504
	v_cvt_pk_bf16_f32 v32, v46, v47
	v_pk_max_i16 v75, v32, 0
	v_cvt_pk_bf16_f32 v32, v56, v57
	v_pk_max_i16 v84, v32, 0
	v_cvt_pk_bf16_f32 v32, v58, v59
	v_pk_max_i16 v85, v32, 0
	s_waitcnt lgkmcnt(6)
	v_mfma_f32_32x32x16_bf16 v[96:111], v[244:247], v[174:177], v[96:111]
	v_cvt_pk_bf16_f32 v32, v60, v61
	v_pk_max_i16 v86, v32, 0
	v_cvt_pk_bf16_f32 v32, v62, v63
	v_pk_max_i16 v87, v32, 0
	v_mfma_f32_32x32x16_bf16 v[112:127], v[244:247], v[80:83], v[112:127]
	s_waitcnt lgkmcnt(5)
	v_mfma_f32_32x32x16_bf16 v[128:143], v[248:251], v[64:67], v[128:143]
	v_mfma_f32_32x32x16_bf16 v[144:159], v[248:251], v[68:71], v[144:159]
	s_waitcnt lgkmcnt(4)
	v_mfma_f32_32x32x16_bf16 v[96:111], v[252:255], v[64:67], v[96:111]
	v_mfma_f32_32x32x16_bf16 v[112:127], v[252:255], v[68:71], v[112:127]
	v_cvt_pk_bf16_f32 v0, v0, v1
	v_pk_max_i16 v206, v0, 0
	v_cvt_pk_bf16_f32 v0, v2, v3
	v_pk_max_i16 v207, v0, 0
	v_cvt_pk_bf16_f32 v0, v4, v5
	s_waitcnt lgkmcnt(2)
	v_mfma_f32_32x32x16_bf16 v[96:111], v[208:211], v[76:79], v[96:111]
	ds_read_b128 v[32:35], v233 offset:24576
	ds_read_b128 v[36:39], v233 offset:25600
	ds_read_b128 v[40:43], v233 offset:28672
	ds_read_b128 v[44:47], v233 offset:29696
	v_mfma_f32_32x32x16_bf16 v[112:127], v[208:211], v[88:91], v[112:127]
	v_pk_max_i16 v208, v0, 0
	v_cvt_pk_bf16_f32 v0, v6, v7
	v_pk_max_i16 v209, v0, 0
	v_cvt_pk_bf16_f32 v0, v16, v17
	v_pk_max_i16 v214, v0, 0
	v_cvt_pk_bf16_f32 v0, v18, v19
	v_pk_max_i16 v215, v0, 0
	v_cvt_pk_bf16_f32 v0, v20, v21
	v_pk_max_i16 v216, v0, 0
	v_cvt_pk_bf16_f32 v0, v22, v23
	v_mfma_f32_32x32x16_bf16 v[128:143], v[92:95], v[76:79], v[128:143]
	v_pk_max_i16 v217, v0, 0
	v_cvt_pk_bf16_f32 v0, v8, v9
	v_mfma_f32_32x32x16_bf16 v[144:159], v[92:95], v[88:91], v[144:159]
	v_pk_max_i16 v92, v0, 0
	v_cvt_pk_bf16_f32 v0, v10, v11
	v_pk_max_i16 v93, v0, 0
	v_cvt_pk_bf16_f32 v0, v12, v13
	v_pk_max_i16 v94, v0, 0
	v_cvt_pk_bf16_f32 v0, v14, v15
	v_pk_max_i16 v95, v0, 0
	v_cvt_pk_bf16_f32 v0, v24, v25
	v_pk_max_i16 v210, v0, 0
	v_cvt_pk_bf16_f32 v0, v26, v27
	v_pk_max_i16 v211, v0, 0
	v_cvt_pk_bf16_f32 v0, v28, v29
	v_pk_max_i16 v212, v0, 0
	v_cvt_pk_bf16_f32 v0, v30, v31
	s_waitcnt lgkmcnt(5)
	v_mfma_f32_32x32x16_bf16 v[128:143], v[236:239], v[72:75], v[128:143]
	v_pk_max_i16 v213, v0, 0
	v_mfma_f32_32x32x16_bf16 v[144:159], v[236:239], v[84:87], v[144:159]
	s_waitcnt lgkmcnt(4)
	v_mfma_f32_32x32x16_bf16 v[96:111], v[240:243], v[72:75], v[96:111]
	v_mfma_f32_32x32x16_bf16 v[112:127], v[240:243], v[84:87], v[112:127]
	s_waitcnt lgkmcnt(3)
	v_mfma_f32_32x32x16_bf16 v[128:143], v[32:35], v[206:209], v[128:143]
	ds_read_b128 v[0:3], v234 offset:51200
	ds_read_b128 v[236:239], v234 offset:52224
	ds_read_b128 v[240:243], v234 offset:55296
	ds_read_b128 v[244:247], v234 offset:56320
	v_mfma_f32_32x32x16_bf16 v[144:159], v[32:35], v[214:217], v[144:159]
	s_waitcnt lgkmcnt(6)
	v_mfma_f32_32x32x16_bf16 v[96:111], v[36:39], v[206:209], v[96:111]
	v_mfma_f32_32x32x16_bf16 v[112:127], v[36:39], v[214:217], v[112:127]
	s_waitcnt lgkmcnt(5)
	v_mfma_f32_32x32x16_bf16 v[128:143], v[40:43], v[92:95], v[128:143]
	v_mfma_f32_32x32x16_bf16 v[144:159], v[40:43], v[210:213], v[144:159]
	s_waitcnt lgkmcnt(4)
	v_mfma_f32_32x32x16_bf16 v[96:111], v[44:47], v[92:95], v[96:111]
	v_mfma_f32_32x32x16_bf16 v[112:127], v[44:47], v[210:213], v[112:127]
	ds_read_b128 v[32:35], v235 offset:256
	ds_read_b128 v[36:39], v235 offset:288
	ds_read_b128 v[40:43], v235 offset:320
	ds_read_b128 v[44:47], v235 offset:352
	s_nop 3
	v_cvt_pk_bf16_f32 v128, v128, v129
	v_cvt_pk_bf16_f32 v129, v130, v131
	v_cvt_pk_bf16_f32 v130, v132, v133
	v_cvt_pk_bf16_f32 v131, v134, v135
	s_waitcnt lgkmcnt(0)
	v_mfma_f32_32x32x16_bf16 v[48:63], v[0:3], v[166:169], v[32:47]
	v_cvt_pk_bf16_f32 v132, v144, v145
	v_cvt_pk_bf16_f32 v133, v146, v147
	v_cvt_pk_bf16_f32 v134, v148, v149
	v_cvt_pk_bf16_f32 v135, v150, v151
	v_pk_max_i16 v128, v128, 0
	v_pk_max_i16 v129, v129, 0
	v_pk_max_i16 v130, v130, 0
	v_mfma_f32_32x32x16_bf16 v[32:47], v[0:3], v[162:165], v[32:47]
	ds_read_b128 v[0:3], v235 offset:384
	ds_read_b128 v[4:7], v235 offset:416
	ds_read_b128 v[8:11], v235 offset:448
	ds_read_b128 v[12:15], v235 offset:480
	v_pk_max_i16 v131, v131, 0
	v_pk_max_i16 v132, v132, 0
	v_pk_max_i16 v133, v133, 0
	v_pk_max_i16 v134, v134, 0
	v_pk_max_i16 v135, v135, 0
	s_waitcnt lgkmcnt(0)
	v_mfma_f32_32x32x16_bf16 v[16:31], v[236:239], v[166:169], v[0:15]
	v_mfma_f32_32x32x16_bf16 v[0:15], v[236:239], v[162:165], v[0:15]
	ds_read_b128 v[162:165], v234 offset:59392
	ds_read_b128 v[166:169], v234 offset:60416
	ds_read_b128 v[236:239], v234 offset:63488
	ds_read_b128 v[248:251], v234 offset:64512
	v_mfma_f32_32x32x16_bf16 v[0:15], v[244:247], v[170:173], v[0:15]
	v_mfma_f32_32x32x16_bf16 v[32:47], v[240:243], v[170:173], v[32:47]
	v_mfma_f32_32x32x16_bf16 v[48:63], v[240:243], v[202:205], v[48:63]
	v_mfma_f32_32x32x16_bf16 v[16:31], v[244:247], v[202:205], v[16:31]
	s_waitcnt lgkmcnt(2)
	v_mfma_f32_32x32x16_bf16 v[0:15], v[166:169], v[174:177], v[0:15]
	v_cvt_pk_bf16_f32 v136, v136, v137
	v_cvt_pk_bf16_f32 v137, v138, v139
	v_cvt_pk_bf16_f32 v138, v140, v141
	v_cvt_pk_bf16_f32 v139, v142, v143
	v_cvt_pk_bf16_f32 v140, v152, v153
	v_pk_max_i16 v136, v136, 0
	v_pk_max_i16 v137, v137, 0
	v_mfma_f32_32x32x16_bf16 v[32:47], v[162:165], v[174:177], v[32:47]
	v_pk_max_i16 v138, v138, 0
	v_pk_max_i16 v139, v139, 0
	v_pk_max_i16 v140, v140, 0
	v_mfma_f32_32x32x16_bf16 v[48:63], v[162:165], v[80:83], v[48:63]
	v_mfma_f32_32x32x16_bf16 v[16:31], v[166:169], v[80:83], v[16:31]
	ds_read_b128 v[80:83], v233 offset:18432
	ds_read_b128 v[144:147], v233 offset:19456
	ds_read_b128 v[148:151], v233 offset:22528
	ds_read_b128 v[162:165], v233 offset:23552
	s_waitcnt lgkmcnt(4)
	v_mfma_f32_32x32x16_bf16 v[0:15], v[248:251], v[64:67], v[0:15]
	v_mfma_f32_32x32x16_bf16 v[32:47], v[236:239], v[64:67], v[32:47]
	v_cvt_pk_bf16_f32 v64, v154, v155
	v_pk_max_i16 v141, v64, 0
	v_cvt_pk_bf16_f32 v64, v156, v157
	v_pk_max_i16 v142, v64, 0
	v_cvt_pk_bf16_f32 v64, v158, v159
	v_pk_max_i16 v143, v64, 0
	v_mfma_f32_32x32x16_bf16 v[48:63], v[236:239], v[68:71], v[48:63]
	v_mfma_f32_32x32x16_bf16 v[16:31], v[248:251], v[68:71], v[16:31]
	s_waitcnt lgkmcnt(2)
	v_mfma_f32_32x32x16_bf16 v[0:15], v[144:147], v[76:79], v[0:15]
	v_mfma_f32_32x32x16_bf16 v[32:47], v[80:83], v[76:79], v[32:47]
	v_mfma_f32_32x32x16_bf16 v[48:63], v[80:83], v[88:91], v[48:63]
	ds_read_b128 v[64:67], v233 offset:26624
	ds_read_b128 v[68:71], v233 offset:27648
	ds_read_b128 v[76:79], v233 offset:30720
	ds_read_b128 v[80:83], v233 offset:31744
	v_mfma_f32_32x32x16_bf16 v[16:31], v[144:147], v[88:91], v[16:31]
	v_cvt_pk_bf16_f32 v88, v96, v97
	v_pk_max_i16 v96, v88, 0
	v_cvt_pk_bf16_f32 v88, v98, v99
	v_pk_max_i16 v97, v88, 0
	v_cvt_pk_bf16_f32 v88, v100, v101
	v_pk_max_i16 v98, v88, 0
	v_cvt_pk_bf16_f32 v88, v102, v103
	s_waitcnt lgkmcnt(4)
	v_mfma_f32_32x32x16_bf16 v[0:15], v[162:165], v[72:75], v[0:15]
	v_pk_max_i16 v99, v88, 0
	v_cvt_pk_bf16_f32 v88, v112, v113
	v_pk_max_i16 v100, v88, 0
	v_mfma_f32_32x32x16_bf16 v[32:47], v[148:151], v[72:75], v[32:47]
	v_cvt_pk_bf16_f32 v72, v114, v115
	v_pk_max_i16 v101, v72, 0
	v_cvt_pk_bf16_f32 v72, v116, v117
	v_pk_max_i16 v102, v72, 0
	v_cvt_pk_bf16_f32 v72, v118, v119
	v_pk_max_i16 v103, v72, 0
	v_mfma_f32_32x32x16_bf16 v[48:63], v[148:151], v[84:87], v[48:63]
	v_mfma_f32_32x32x16_bf16 v[16:31], v[162:165], v[84:87], v[16:31]
	s_waitcnt lgkmcnt(2)
	v_mfma_f32_32x32x16_bf16 v[0:15], v[68:71], v[206:209], v[0:15]
	ds_read_b128 v[84:87], v160
	ds_read_b128 v[112:115], v160 offset:1024
	ds_read_b128 v[116:119], v160 offset:2048
	ds_read_b128 v[144:147], v160 offset:3072
	v_mfma_f32_32x32x16_bf16 v[32:47], v[64:67], v[206:209], v[32:47]
	v_mfma_f32_32x32x16_bf16 v[48:63], v[64:67], v[214:217], v[48:63]
	v_cvt_pk_bf16_f32 v64, v104, v105
	v_pk_max_i16 v104, v64, 0
	v_cvt_pk_bf16_f32 v64, v106, v107
	v_pk_max_i16 v105, v64, 0
	v_cvt_pk_bf16_f32 v64, v108, v109
	v_pk_max_i16 v106, v64, 0
	v_cvt_pk_bf16_f32 v64, v110, v111
	v_mfma_f32_32x32x16_bf16 v[16:31], v[68:71], v[214:217], v[16:31]
	v_pk_max_i16 v107, v64, 0
	v_cvt_pk_bf16_f32 v64, v120, v121
	v_pk_max_i16 v108, v64, 0
	v_cvt_pk_bf16_f32 v64, v122, v123
	v_pk_max_i16 v109, v64, 0
	v_cvt_pk_bf16_f32 v64, v124, v125
	v_pk_max_i16 v110, v64, 0
	s_waitcnt lgkmcnt(4)
	v_mfma_f32_32x32x16_bf16 v[0:15], v[80:83], v[92:95], v[0:15]
	v_cvt_pk_bf16_f32 v64, v126, v127
	v_pk_max_i16 v111, v64, 0
	v_mfma_f32_32x32x16_bf16 v[32:47], v[76:79], v[92:95], v[32:47]
	v_mfma_f32_32x32x16_bf16 v[48:63], v[76:79], v[210:213], v[48:63]
	v_mfma_f32_32x32x16_bf16 v[16:31], v[80:83], v[210:213], v[16:31]
	s_waitcnt lgkmcnt(3)
	v_mfma_f32_32x32x16_bf16 v[64:79], v[84:87], v[128:131], 0
	s_nop 7
	v_cvt_pk_bf16_f32 v32, v32, v33
	v_cvt_pk_bf16_f32 v33, v34, v35
	v_cvt_pk_bf16_f32 v34, v36, v37
	v_cvt_pk_bf16_f32 v35, v38, v39
	v_pk_max_i16 v32, v32, 0
	v_pk_max_i16 v33, v33, 0
	v_pk_max_i16 v34, v34, 0
	v_mfma_f32_32x32x16_bf16 v[80:95], v[84:87], v[132:135], 0
	v_pk_max_i16 v35, v35, 0
	v_cvt_pk_bf16_f32 v48, v48, v49
	v_cvt_pk_bf16_f32 v49, v50, v51
	v_cvt_pk_bf16_f32 v50, v52, v53
	v_cvt_pk_bf16_f32 v51, v54, v55
	v_pk_max_i16 v48, v48, 0
	v_pk_max_i16 v49, v49, 0
	s_waitcnt lgkmcnt(2)
	v_mfma_f32_32x32x16_bf16 v[64:79], v[112:115], v[136:139], v[64:79]
	v_pk_max_i16 v50, v50, 0
	v_pk_max_i16 v51, v51, 0
	v_cvt_pk_bf16_f32 v40, v40, v41
	v_cvt_pk_bf16_f32 v41, v42, v43
	v_cvt_pk_bf16_f32 v42, v44, v45
	v_cvt_pk_bf16_f32 v43, v46, v47
	v_pk_max_i16 v40, v40, 0
	v_mfma_f32_32x32x16_bf16 v[80:95], v[112:115], v[140:143], v[80:95]
	v_pk_max_i16 v41, v41, 0
	v_pk_max_i16 v42, v42, 0
	v_pk_max_i16 v43, v43, 0
	v_cvt_pk_bf16_f32 v52, v56, v57
	v_cvt_pk_bf16_f32 v53, v58, v59
	v_cvt_pk_bf16_f32 v54, v60, v61
	v_cvt_pk_bf16_f32 v55, v62, v63
	s_waitcnt lgkmcnt(1)
	v_mfma_f32_32x32x16_bf16 v[64:79], v[116:119], v[96:99], v[64:79]
	ds_read_b128 v[36:39], v160 offset:4096
	ds_read_b128 v[96:99], v160 offset:5120
	v_cvt_pk_bf16_f32 v0, v0, v1
	v_cvt_pk_bf16_f32 v1, v2, v3
	v_cvt_pk_bf16_f32 v2, v4, v5
	v_cvt_pk_bf16_f32 v3, v6, v7
	v_pk_max_i16 v0, v0, 0
	v_pk_max_i16 v1, v1, 0
	v_mfma_f32_32x32x16_bf16 v[80:95], v[116:119], v[100:103], v[80:95]
	v_pk_max_i16 v2, v2, 0
	v_pk_max_i16 v3, v3, 0
	ds_read_b128 v[4:7], v160 offset:7168
	v_cvt_pk_bf16_f32 v12, v12, v13
	v_cvt_pk_bf16_f32 v13, v14, v15
	v_cvt_pk_bf16_f32 v24, v24, v25
	v_cvt_pk_bf16_f32 v25, v26, v27
	s_waitcnt lgkmcnt(3)
	v_mfma_f32_32x32x16_bf16 v[64:79], v[144:147], v[104:107], v[64:79]
	v_cvt_pk_bf16_f32 v26, v28, v29
	v_cvt_pk_bf16_f32 v27, v30, v31
	v_cndmask_b32_e64 v219, v219, 0, s[14:15]
	v_cndmask_b32_e64 v218, v218, 0, s[14:15]
	v_mfma_f32_32x32x16_bf16 v[80:95], v[144:147], v[108:111], v[80:95]
	s_waitcnt lgkmcnt(2)
	v_mfma_f32_32x32x16_bf16 v[64:79], v[36:39], v[32:35], v[64:79]
	v_cvt_pk_bf16_f32 v34, v20, v21
	v_cvt_pk_bf16_f32 v35, v22, v23
	ds_read_b128 v[20:23], v160 offset:6144
	v_cvt_pk_bf16_f32 v32, v16, v17
	v_cvt_pk_bf16_f32 v33, v18, v19
	v_pk_max_i16 v16, v52, 0
	v_pk_max_i16 v17, v53, 0
	v_mfma_f32_32x32x16_bf16 v[80:95], v[36:39], v[48:51], v[80:95]
	v_pk_max_i16 v18, v54, 0
	v_pk_max_i16 v19, v55, 0
	s_waitcnt lgkmcnt(2)
	v_mfma_f32_32x32x16_bf16 v[64:79], v[96:99], v[40:43], v[64:79]
	v_mfma_f32_32x32x16_bf16 v[80:95], v[96:99], v[16:19], v[80:95]
	v_cvt_pk_bf16_f32 v16, v8, v9
	v_cvt_pk_bf16_f32 v17, v10, v11
	v_pk_max_i16 v8, v24, 0
	v_pk_max_i16 v9, v25, 0
	v_pk_max_i16 v10, v26, 0
	v_pk_max_i16 v11, v27, 0
	s_waitcnt lgkmcnt(0)
	v_mfma_f32_32x32x16_bf16 v[64:79], v[20:23], v[0:3], v[64:79]
	v_pk_max_i16 v0, v32, 0
	v_pk_max_i16 v1, v33, 0
	v_pk_max_i16 v2, v34, 0
	v_pk_max_i16 v3, v35, 0
	s_nop 1
	v_mfma_f32_32x32x16_bf16 v[80:95], v[20:23], v[0:3], v[80:95]
	v_pk_max_i16 v0, v16, 0
	v_pk_max_i16 v1, v17, 0
	v_pk_max_i16 v2, v12, 0
	v_pk_max_i16 v3, v13, 0
	s_nop 1
	v_mfma_f32_32x32x16_bf16 v[64:79], v[4:7], v[0:3], v[64:79]
	v_mfma_f32_32x32x16_bf16 v[80:95], v[4:7], v[8:11], v[80:95]
	s_waitcnt vmcnt(10)
	s_nop 7
	s_nop 2
	v_permlane32_swap_b32_e32 v64, v80
	v_permlane32_swap_b32_e32 v65, v81
	v_permlane32_swap_b32_e32 v66, v82
	s_nop 0
	v_add_f32_e32 v3, s10, v64
	v_add_f32_e32 v4, s11, v65
	v_add_f32_e32 v5, s18, v66
	v_mul_f32_e32 v3, 0xbfb8aa3b, v3
	v_mul_f32_e32 v4, 0xbfb8aa3b, v4
	v_mul_f32_e32 v5, 0xbfb8aa3b, v5
	v_exp_f32_e32 v3, v3
	v_exp_f32_e32 v4, v4
	v_exp_f32_e32 v5, v5
	v_add_f32_e32 v3, 1.0, v3
	v_add_f32_e32 v4, 1.0, v4
	v_add_f32_e32 v5, 1.0, v5
	v_rcp_f32_e32 v3, v3
	v_rcp_f32_e32 v4, v4
	v_rcp_f32_e32 v5, v5
	v_fmac_f32_e32 v218, v232, v3
	v_fmac_f32_e32 v219, v232, v4
	v_fmac_f32_e32 v230, v232, v5
	s_andn2_b64 vcc, exec, s[12:13]
	s_cbranch_vccnz .LBB1_6
	v_and_b32_e32 v1, 64, v229
	v_xor_b32_e32 v0, 32, v229
	v_add_u32_e32 v2, 64, v1
	v_cmp_lt_i32_e32 vcc, v0, v2
	s_nop 1
	v_cndmask_b32_e32 v0, v229, v0, vcc
	v_lshlrev_b32_e32 v0, 2, v0
	s_waitcnt lgkmcnt(0)
	ds_bpermute_b32 v1, v0, v230
	v_xor_b32_e32 v3, 16, v229
	v_cmp_lt_i32_e32 vcc, v3, v2
	ds_bpermute_b32 v4, v0, v218
	ds_bpermute_b32 v5, v0, v219
	v_cndmask_b32_e32 v3, v229, v3, vcc
	v_lshlrev_b32_e32 v3, 2, v3
	s_waitcnt lgkmcnt(2)
	v_add_f32_e32 v1, v230, v1
	ds_bpermute_b32 v6, v3, v1
	v_xor_b32_e32 v0, 8, v229
	v_cmp_lt_i32_e32 vcc, v0, v2
	v_xor_b32_e32 v9, 4, v229
	s_waitcnt lgkmcnt(0)
	v_add_f32_e32 v6, v1, v6
	v_cndmask_b32_e32 v0, v229, v0, vcc
	v_lshlrev_b32_e32 v7, 2, v0
	v_pk_add_f32 v[0:1], v[218:219], v[4:5]
	ds_bpermute_b32 v4, v3, v0
	ds_bpermute_b32 v5, v3, v1
	ds_bpermute_b32 v8, v7, v6
	v_cmp_lt_i32_e32 vcc, v9, v2
	s_waitcnt lgkmcnt(1)
	v_pk_add_f32 v[0:1], v[0:1], v[4:5]
	ds_bpermute_b32 v4, v7, v0
	ds_bpermute_b32 v5, v7, v1
	v_cndmask_b32_e32 v3, v229, v9, vcc
	s_waitcnt lgkmcnt(2)
	v_add_f32_e32 v6, v6, v8
	v_lshlrev_b32_e32 v3, 2, v3
	ds_bpermute_b32 v8, v3, v6
	s_waitcnt lgkmcnt(1)
	v_pk_add_f32 v[0:1], v[0:1], v[4:5]
	ds_bpermute_b32 v4, v3, v0
	ds_bpermute_b32 v5, v3, v1
	v_xor_b32_e32 v3, 2, v229
	v_cmp_lt_i32_e32 vcc, v3, v2
	s_waitcnt lgkmcnt(2)
	v_add_f32_e32 v6, v6, v8
	s_waitcnt lgkmcnt(0)
	v_pk_add_f32 v[0:1], v[0:1], v[4:5]
	v_cndmask_b32_e32 v3, v229, v3, vcc
	v_lshlrev_b32_e32 v3, 2, v3
	ds_bpermute_b32 v4, v3, v0
	ds_bpermute_b32 v5, v3, v1
	ds_bpermute_b32 v3, v3, v6
	s_waitcnt lgkmcnt(1)
	v_pk_add_f32 v[0:1], v[0:1], v[4:5]
	s_waitcnt lgkmcnt(0)
	v_add_f32_e32 v4, v6, v3
	v_xor_b32_e32 v3, 1, v229
	v_cmp_lt_i32_e32 vcc, v3, v2
	s_nop 1
	v_cndmask_b32_e32 v2, v229, v3, vcc
	v_lshlrev_b32_e32 v5, 2, v2
	ds_bpermute_b32 v2, v5, v0
	ds_bpermute_b32 v3, v5, v1
	ds_bpermute_b32 v5, v5, v4
	s_and_saveexec_b64 s[12:13], s[2:3]
	s_cbranch_execz .LBB1_5
	v_lshl_add_u32 v6, v231, 1, v231
	v_ashrrev_i32_e32 v7, 31, v6
	s_waitcnt lgkmcnt(0)
	v_add_f32_e32 v4, v4, v5
	v_lshl_add_u64 v[6:7], v[6:7], 2, s[8:9]
	v_pk_add_f32 v[2:3], v[0:1], v[2:3]
	global_store_dwordx3 v[6:7], v[2:4], off
	s_branch .LBB1_5
